# V^T transpose loop: 16 loads in flight instead of one load per round trip
# baseline (speedup 1.0000x reference)
.LBB0_234:
	v_ashrrev_i32_e32 v6, 20, v0
	v_ashrrev_i32_e32 v7, 31, v6
	v_lshlrev_b64 v[6:7], 10, v[6:7]
	v_lshrrev_b32_e32 v1, 10, v0
	s_movk_i32 s10, 0x300
	v_and_or_b32 v1, v1, s10, v6
	v_or_b32_e32 v6, v1, v2
	v_lshlrev_b64 v[6:7], 12, v[6:7]
	v_lshrrev_b32_e32 v1, 7, v0
	v_lshl_add_u64 v[6:7], s[90:91], 0, v[6:7]
	v_and_b32_e32 v144, 0x600, v1
	v_lshl_add_u64 v[6:7], v[6:7], 0, v[144:145]
	v_lshlrev_b32_sdwa v144, v197, v0 dst_sel:DWORD dst_unused:UNUSED_PAD src0_sel:DWORD src1_sel:BYTE_1
	v_lshl_add_u64 v[6:7], v[6:7], 0, v[144:145]
	global_load_ushort v8, v[6:7], off offset:2048
	v_add_u32_e32 v0, s14, v0
	v_ashrrev_i32_e32 v6, 20, v0
	v_ashrrev_i32_e32 v7, 31, v6
	v_lshlrev_b64 v[6:7], 10, v[6:7]
	v_lshrrev_b32_e32 v1, 10, v0
	s_movk_i32 s10, 0x300
	v_and_or_b32 v1, v1, s10, v6
	v_or_b32_e32 v6, v1, v2
	v_lshlrev_b64 v[6:7], 12, v[6:7]
	v_lshrrev_b32_e32 v1, 7, v0
	v_lshl_add_u64 v[6:7], s[90:91], 0, v[6:7]
	v_and_b32_e32 v144, 0x600, v1
	v_lshl_add_u64 v[6:7], v[6:7], 0, v[144:145]
	v_lshlrev_b32_sdwa v144, v197, v0 dst_sel:DWORD dst_unused:UNUSED_PAD src0_sel:DWORD src1_sel:BYTE_1
	v_lshl_add_u64 v[6:7], v[6:7], 0, v[144:145]
	global_load_ushort v9, v[6:7], off offset:2048
	v_add_u32_e32 v0, s14, v0
	v_ashrrev_i32_e32 v6, 20, v0
	v_ashrrev_i32_e32 v7, 31, v6
	v_lshlrev_b64 v[6:7], 10, v[6:7]
	v_lshrrev_b32_e32 v1, 10, v0
	s_movk_i32 s10, 0x300
	v_and_or_b32 v1, v1, s10, v6
	v_or_b32_e32 v6, v1, v2
	v_lshlrev_b64 v[6:7], 12, v[6:7]
	v_lshrrev_b32_e32 v1, 7, v0
	v_lshl_add_u64 v[6:7], s[90:91], 0, v[6:7]
	v_and_b32_e32 v144, 0x600, v1
	v_lshl_add_u64 v[6:7], v[6:7], 0, v[144:145]
	v_lshlrev_b32_sdwa v144, v197, v0 dst_sel:DWORD dst_unused:UNUSED_PAD src0_sel:DWORD src1_sel:BYTE_1
	v_lshl_add_u64 v[6:7], v[6:7], 0, v[144:145]
	global_load_ushort v10, v[6:7], off offset:2048
	v_add_u32_e32 v0, s14, v0
	v_ashrrev_i32_e32 v6, 20, v0
	v_ashrrev_i32_e32 v7, 31, v6
	v_lshlrev_b64 v[6:7], 10, v[6:7]
	v_lshrrev_b32_e32 v1, 10, v0
	s_movk_i32 s10, 0x300
	v_and_or_b32 v1, v1, s10, v6
	v_or_b32_e32 v6, v1, v2
	v_lshlrev_b64 v[6:7], 12, v[6:7]
	v_lshrrev_b32_e32 v1, 7, v0
	v_lshl_add_u64 v[6:7], s[90:91], 0, v[6:7]
	v_and_b32_e32 v144, 0x600, v1
	v_lshl_add_u64 v[6:7], v[6:7], 0, v[144:145]
	v_lshlrev_b32_sdwa v144, v197, v0 dst_sel:DWORD dst_unused:UNUSED_PAD src0_sel:DWORD src1_sel:BYTE_1
	v_lshl_add_u64 v[6:7], v[6:7], 0, v[144:145]
	global_load_ushort v11, v[6:7], off offset:2048
	v_add_u32_e32 v0, s14, v0
	v_ashrrev_i32_e32 v6, 20, v0
	v_ashrrev_i32_e32 v7, 31, v6
	v_lshlrev_b64 v[6:7], 10, v[6:7]
	v_lshrrev_b32_e32 v1, 10, v0
	s_movk_i32 s10, 0x300
	v_and_or_b32 v1, v1, s10, v6
	v_or_b32_e32 v6, v1, v2
	v_lshlrev_b64 v[6:7], 12, v[6:7]
	v_lshrrev_b32_e32 v1, 7, v0
	v_lshl_add_u64 v[6:7], s[90:91], 0, v[6:7]
	v_and_b32_e32 v144, 0x600, v1
	v_lshl_add_u64 v[6:7], v[6:7], 0, v[144:145]
	v_lshlrev_b32_sdwa v144, v197, v0 dst_sel:DWORD dst_unused:UNUSED_PAD src0_sel:DWORD src1_sel:BYTE_1
	v_lshl_add_u64 v[6:7], v[6:7], 0, v[144:145]
	global_load_ushort v12, v[6:7], off offset:2048
	v_add_u32_e32 v0, s14, v0
	v_ashrrev_i32_e32 v6, 20, v0
	v_ashrrev_i32_e32 v7, 31, v6
	v_lshlrev_b64 v[6:7], 10, v[6:7]
	v_lshrrev_b32_e32 v1, 10, v0
	s_movk_i32 s10, 0x300
	v_and_or_b32 v1, v1, s10, v6
	v_or_b32_e32 v6, v1, v2
	v_lshlrev_b64 v[6:7], 12, v[6:7]
	v_lshrrev_b32_e32 v1, 7, v0
	v_lshl_add_u64 v[6:7], s[90:91], 0, v[6:7]
	v_and_b32_e32 v144, 0x600, v1
	v_lshl_add_u64 v[6:7], v[6:7], 0, v[144:145]
	v_lshlrev_b32_sdwa v144, v197, v0 dst_sel:DWORD dst_unused:UNUSED_PAD src0_sel:DWORD src1_sel:BYTE_1
	v_lshl_add_u64 v[6:7], v[6:7], 0, v[144:145]
	global_load_ushort v13, v[6:7], off offset:2048
	v_add_u32_e32 v0, s14, v0
	v_ashrrev_i32_e32 v6, 20, v0
	v_ashrrev_i32_e32 v7, 31, v6
	v_lshlrev_b64 v[6:7], 10, v[6:7]
	v_lshrrev_b32_e32 v1, 10, v0
	s_movk_i32 s10, 0x300
	v_and_or_b32 v1, v1, s10, v6
	v_or_b32_e32 v6, v1, v2
	v_lshlrev_b64 v[6:7], 12, v[6:7]
	v_lshrrev_b32_e32 v1, 7, v0
	v_lshl_add_u64 v[6:7], s[90:91], 0, v[6:7]
	v_and_b32_e32 v144, 0x600, v1
	v_lshl_add_u64 v[6:7], v[6:7], 0, v[144:145]
	v_lshlrev_b32_sdwa v144, v197, v0 dst_sel:DWORD dst_unused:UNUSED_PAD src0_sel:DWORD src1_sel:BYTE_1
	v_lshl_add_u64 v[6:7], v[6:7], 0, v[144:145]
	global_load_ushort v14, v[6:7], off offset:2048
	v_add_u32_e32 v0, s14, v0
	v_ashrrev_i32_e32 v6, 20, v0
	v_ashrrev_i32_e32 v7, 31, v6
	v_lshlrev_b64 v[6:7], 10, v[6:7]
	v_lshrrev_b32_e32 v1, 10, v0
	s_movk_i32 s10, 0x300
	v_and_or_b32 v1, v1, s10, v6
	v_or_b32_e32 v6, v1, v2
	v_lshlrev_b64 v[6:7], 12, v[6:7]
	v_lshrrev_b32_e32 v1, 7, v0
	v_lshl_add_u64 v[6:7], s[90:91], 0, v[6:7]
	v_and_b32_e32 v144, 0x600, v1
	v_lshl_add_u64 v[6:7], v[6:7], 0, v[144:145]
	v_lshlrev_b32_sdwa v144, v197, v0 dst_sel:DWORD dst_unused:UNUSED_PAD src0_sel:DWORD src1_sel:BYTE_1
	v_lshl_add_u64 v[6:7], v[6:7], 0, v[144:145]
	global_load_ushort v15, v[6:7], off offset:2048
	v_add_u32_e32 v0, s14, v0
	v_ashrrev_i32_e32 v6, 20, v0
	v_ashrrev_i32_e32 v7, 31, v6
	v_lshlrev_b64 v[6:7], 10, v[6:7]
	v_lshrrev_b32_e32 v1, 10, v0
	s_movk_i32 s10, 0x300
	v_and_or_b32 v1, v1, s10, v6
	v_or_b32_e32 v6, v1, v2
	v_lshlrev_b64 v[6:7], 12, v[6:7]
	v_lshrrev_b32_e32 v1, 7, v0
	v_lshl_add_u64 v[6:7], s[90:91], 0, v[6:7]
	v_and_b32_e32 v144, 0x600, v1
	v_lshl_add_u64 v[6:7], v[6:7], 0, v[144:145]
	v_lshlrev_b32_sdwa v144, v197, v0 dst_sel:DWORD dst_unused:UNUSED_PAD src0_sel:DWORD src1_sel:BYTE_1
	v_lshl_add_u64 v[6:7], v[6:7], 0, v[144:145]
	global_load_ushort v16, v[6:7], off offset:2048
	v_add_u32_e32 v0, s14, v0
	v_ashrrev_i32_e32 v6, 20, v0
	v_ashrrev_i32_e32 v7, 31, v6
	v_lshlrev_b64 v[6:7], 10, v[6:7]
	v_lshrrev_b32_e32 v1, 10, v0
	s_movk_i32 s10, 0x300
	v_and_or_b32 v1, v1, s10, v6
	v_or_b32_e32 v6, v1, v2
	v_lshlrev_b64 v[6:7], 12, v[6:7]
	v_lshrrev_b32_e32 v1, 7, v0
	v_lshl_add_u64 v[6:7], s[90:91], 0, v[6:7]
	v_and_b32_e32 v144, 0x600, v1
	v_lshl_add_u64 v[6:7], v[6:7], 0, v[144:145]
	v_lshlrev_b32_sdwa v144, v197, v0 dst_sel:DWORD dst_unused:UNUSED_PAD src0_sel:DWORD src1_sel:BYTE_1
	v_lshl_add_u64 v[6:7], v[6:7], 0, v[144:145]
	global_load_ushort v17, v[6:7], off offset:2048
	v_add_u32_e32 v0, s14, v0
	v_ashrrev_i32_e32 v6, 20, v0
	v_ashrrev_i32_e32 v7, 31, v6
	v_lshlrev_b64 v[6:7], 10, v[6:7]
	v_lshrrev_b32_e32 v1, 10, v0
	s_movk_i32 s10, 0x300
	v_and_or_b32 v1, v1, s10, v6
	v_or_b32_e32 v6, v1, v2
	v_lshlrev_b64 v[6:7], 12, v[6:7]
	v_lshrrev_b32_e32 v1, 7, v0
	v_lshl_add_u64 v[6:7], s[90:91], 0, v[6:7]
	v_and_b32_e32 v144, 0x600, v1
	v_lshl_add_u64 v[6:7], v[6:7], 0, v[144:145]
	v_lshlrev_b32_sdwa v144, v197, v0 dst_sel:DWORD dst_unused:UNUSED_PAD src0_sel:DWORD src1_sel:BYTE_1
	v_lshl_add_u64 v[6:7], v[6:7], 0, v[144:145]
	global_load_ushort v18, v[6:7], off offset:2048
	v_add_u32_e32 v0, s14, v0
	v_ashrrev_i32_e32 v6, 20, v0
	v_ashrrev_i32_e32 v7, 31, v6
	v_lshlrev_b64 v[6:7], 10, v[6:7]
	v_lshrrev_b32_e32 v1, 10, v0
	s_movk_i32 s10, 0x300
	v_and_or_b32 v1, v1, s10, v6
	v_or_b32_e32 v6, v1, v2
	v_lshlrev_b64 v[6:7], 12, v[6:7]
	v_lshrrev_b32_e32 v1, 7, v0
	v_lshl_add_u64 v[6:7], s[90:91], 0, v[6:7]
	v_and_b32_e32 v144, 0x600, v1
	v_lshl_add_u64 v[6:7], v[6:7], 0, v[144:145]
	v_lshlrev_b32_sdwa v144, v197, v0 dst_sel:DWORD dst_unused:UNUSED_PAD src0_sel:DWORD src1_sel:BYTE_1
	v_lshl_add_u64 v[6:7], v[6:7], 0, v[144:145]
	global_load_ushort v19, v[6:7], off offset:2048
	v_add_u32_e32 v0, s14, v0
	v_ashrrev_i32_e32 v6, 20, v0
	v_ashrrev_i32_e32 v7, 31, v6
	v_lshlrev_b64 v[6:7], 10, v[6:7]
	v_lshrrev_b32_e32 v1, 10, v0
	s_movk_i32 s10, 0x300
	v_and_or_b32 v1, v1, s10, v6
	v_or_b32_e32 v6, v1, v2
	v_lshlrev_b64 v[6:7], 12, v[6:7]
	v_lshrrev_b32_e32 v1, 7, v0
	v_lshl_add_u64 v[6:7], s[90:91], 0, v[6:7]
	v_and_b32_e32 v144, 0x600, v1
	v_lshl_add_u64 v[6:7], v[6:7], 0, v[144:145]
	v_lshlrev_b32_sdwa v144, v197, v0 dst_sel:DWORD dst_unused:UNUSED_PAD src0_sel:DWORD src1_sel:BYTE_1
	v_lshl_add_u64 v[6:7], v[6:7], 0, v[144:145]
	global_load_ushort v20, v[6:7], off offset:2048
	v_add_u32_e32 v0, s14, v0
	v_ashrrev_i32_e32 v6, 20, v0
	v_ashrrev_i32_e32 v7, 31, v6
	v_lshlrev_b64 v[6:7], 10, v[6:7]
	v_lshrrev_b32_e32 v1, 10, v0
	s_movk_i32 s10, 0x300
	v_and_or_b32 v1, v1, s10, v6
	v_or_b32_e32 v6, v1, v2
	v_lshlrev_b64 v[6:7], 12, v[6:7]
	v_lshrrev_b32_e32 v1, 7, v0
	v_lshl_add_u64 v[6:7], s[90:91], 0, v[6:7]
	v_and_b32_e32 v144, 0x600, v1
	v_lshl_add_u64 v[6:7], v[6:7], 0, v[144:145]
	v_lshlrev_b32_sdwa v144, v197, v0 dst_sel:DWORD dst_unused:UNUSED_PAD src0_sel:DWORD src1_sel:BYTE_1
	v_lshl_add_u64 v[6:7], v[6:7], 0, v[144:145]
	global_load_ushort v21, v[6:7], off offset:2048
	v_add_u32_e32 v0, s14, v0
	v_ashrrev_i32_e32 v6, 20, v0
	v_ashrrev_i32_e32 v7, 31, v6
	v_lshlrev_b64 v[6:7], 10, v[6:7]
	v_lshrrev_b32_e32 v1, 10, v0
	s_movk_i32 s10, 0x300
	v_and_or_b32 v1, v1, s10, v6
	v_or_b32_e32 v6, v1, v2
	v_lshlrev_b64 v[6:7], 12, v[6:7]
	v_lshrrev_b32_e32 v1, 7, v0
	v_lshl_add_u64 v[6:7], s[90:91], 0, v[6:7]
	v_and_b32_e32 v144, 0x600, v1
	v_lshl_add_u64 v[6:7], v[6:7], 0, v[144:145]
	v_lshlrev_b32_sdwa v144, v197, v0 dst_sel:DWORD dst_unused:UNUSED_PAD src0_sel:DWORD src1_sel:BYTE_1
	v_lshl_add_u64 v[6:7], v[6:7], 0, v[144:145]
	global_load_ushort v22, v[6:7], off offset:2048
	v_add_u32_e32 v0, s14, v0
	v_ashrrev_i32_e32 v6, 20, v0
	v_ashrrev_i32_e32 v7, 31, v6
	v_lshlrev_b64 v[6:7], 10, v[6:7]
	v_lshrrev_b32_e32 v1, 10, v0
	s_movk_i32 s10, 0x300
	v_and_or_b32 v1, v1, s10, v6
	v_or_b32_e32 v6, v1, v2
	v_lshlrev_b64 v[6:7], 12, v[6:7]
	v_lshrrev_b32_e32 v1, 7, v0
	v_lshl_add_u64 v[6:7], s[90:91], 0, v[6:7]
	v_and_b32_e32 v144, 0x600, v1
	v_lshl_add_u64 v[6:7], v[6:7], 0, v[144:145]
	v_lshlrev_b32_sdwa v144, v197, v0 dst_sel:DWORD dst_unused:UNUSED_PAD src0_sel:DWORD src1_sel:BYTE_1
	v_lshl_add_u64 v[6:7], v[6:7], 0, v[144:145]
	global_load_ushort v23, v[6:7], off offset:2048
	v_add_u32_e32 v0, s14, v0
	s_waitcnt vmcnt(0)
	global_store_short v[4:5], v8, off
	v_lshl_add_u64 v[4:5], v[4:5], 0, s[18:19]
	global_store_short v[4:5], v9, off
	v_lshl_add_u64 v[4:5], v[4:5], 0, s[18:19]
	global_store_short v[4:5], v10, off
	v_lshl_add_u64 v[4:5], v[4:5], 0, s[18:19]
	global_store_short v[4:5], v11, off
	v_lshl_add_u64 v[4:5], v[4:5], 0, s[18:19]
	global_store_short v[4:5], v12, off
	v_lshl_add_u64 v[4:5], v[4:5], 0, s[18:19]
	global_store_short v[4:5], v13, off
	v_lshl_add_u64 v[4:5], v[4:5], 0, s[18:19]
	global_store_short v[4:5], v14, off
	v_lshl_add_u64 v[4:5], v[4:5], 0, s[18:19]
	global_store_short v[4:5], v15, off
	v_lshl_add_u64 v[4:5], v[4:5], 0, s[18:19]
	global_store_short v[4:5], v16, off
	v_lshl_add_u64 v[4:5], v[4:5], 0, s[18:19]
	global_store_short v[4:5], v17, off
	v_lshl_add_u64 v[4:5], v[4:5], 0, s[18:19]
	global_store_short v[4:5], v18, off
	v_lshl_add_u64 v[4:5], v[4:5], 0, s[18:19]
	global_store_short v[4:5], v19, off
	v_lshl_add_u64 v[4:5], v[4:5], 0, s[18:19]
	global_store_short v[4:5], v20, off
	v_lshl_add_u64 v[4:5], v[4:5], 0, s[18:19]
	global_store_short v[4:5], v21, off
	v_lshl_add_u64 v[4:5], v[4:5], 0, s[18:19]
	global_store_short v[4:5], v22, off
	v_lshl_add_u64 v[4:5], v[4:5], 0, s[18:19]
	global_store_short v[4:5], v23, off
	v_lshl_add_u64 v[4:5], v[4:5], 0, s[18:19]
